# b3 + GEMM accumulator zeroing with v_mov_b64 (64 instead of 128 moves per unit)
# speedup vs baseline: 1.0128x; 1.0029x over previous
.LBB0_197:
	s_add_u32 s3, s20, 0x100
	s_addc_u32 s46, s21, 0
	s_add_u32 s18, s18, 0x80080
	v_mov_b32_e32 v4, 0
	s_addc_u32 s19, s19, 0
	s_mov_b32 s48, -2
	v_mov_b32_e32 v5, v4
	v_mov_b64_e32 v[6:7], v[4:5]
	v_mov_b64_e32 v[8:9], v[4:5]
	v_mov_b64_e32 v[10:11], v[4:5]
	v_mov_b64_e32 v[20:21], v[4:5]
	v_mov_b64_e32 v[22:23], v[4:5]
	v_mov_b64_e32 v[24:25], v[4:5]
	v_mov_b64_e32 v[26:27], v[4:5]
	v_mov_b64_e32 v[36:37], v[4:5]
	v_mov_b64_e32 v[38:39], v[4:5]
	v_mov_b64_e32 v[40:41], v[4:5]
	v_mov_b64_e32 v[42:43], v[4:5]
	v_mov_b64_e32 v[52:53], v[4:5]
	v_mov_b64_e32 v[54:55], v[4:5]
	v_mov_b64_e32 v[56:57], v[4:5]
	v_mov_b64_e32 v[58:59], v[4:5]
	v_mov_b64_e32 v[12:13], v[4:5]
	v_mov_b64_e32 v[14:15], v[4:5]
	v_mov_b64_e32 v[16:17], v[4:5]
	v_mov_b64_e32 v[18:19], v[4:5]
	v_mov_b64_e32 v[28:29], v[4:5]
	v_mov_b64_e32 v[30:31], v[4:5]
	v_mov_b64_e32 v[32:33], v[4:5]
	v_mov_b64_e32 v[34:35], v[4:5]
	v_mov_b64_e32 v[44:45], v[4:5]
	v_mov_b64_e32 v[46:47], v[4:5]
	v_mov_b64_e32 v[48:49], v[4:5]
	v_mov_b64_e32 v[50:51], v[4:5]
	v_mov_b64_e32 v[60:61], v[4:5]
	v_mov_b64_e32 v[62:63], v[4:5]
	v_mov_b64_e32 v[64:65], v[4:5]
	v_mov_b64_e32 v[66:67], v[4:5]
	v_mov_b64_e32 v[68:69], v[4:5]
	v_mov_b64_e32 v[70:71], v[4:5]
	v_mov_b64_e32 v[72:73], v[4:5]
	v_mov_b64_e32 v[74:75], v[4:5]
	v_mov_b64_e32 v[84:85], v[4:5]
	v_mov_b64_e32 v[86:87], v[4:5]
	v_mov_b64_e32 v[88:89], v[4:5]
	v_mov_b64_e32 v[90:91], v[4:5]
	v_mov_b64_e32 v[100:101], v[4:5]
	v_mov_b64_e32 v[102:103], v[4:5]
	v_mov_b64_e32 v[104:105], v[4:5]
	v_mov_b64_e32 v[106:107], v[4:5]
	v_mov_b64_e32 v[116:117], v[4:5]
	v_mov_b64_e32 v[118:119], v[4:5]
	v_mov_b64_e32 v[120:121], v[4:5]
	v_mov_b64_e32 v[122:123], v[4:5]
	v_mov_b64_e32 v[76:77], v[4:5]
	v_mov_b64_e32 v[78:79], v[4:5]
	v_mov_b64_e32 v[80:81], v[4:5]
	v_mov_b64_e32 v[82:83], v[4:5]
	v_mov_b64_e32 v[92:93], v[4:5]
	v_mov_b64_e32 v[94:95], v[4:5]
	v_mov_b64_e32 v[96:97], v[4:5]
	v_mov_b64_e32 v[98:99], v[4:5]
	v_mov_b64_e32 v[108:109], v[4:5]
	v_mov_b64_e32 v[110:111], v[4:5]
	v_mov_b64_e32 v[112:113], v[4:5]
	v_mov_b64_e32 v[114:115], v[4:5]
	v_mov_b64_e32 v[124:125], v[4:5]
	v_mov_b64_e32 v[126:127], v[4:5]
	v_mov_b64_e32 v[128:129], v[4:5]
	v_mov_b64_e32 v[130:131], v[4:5]

.LBB0_235:
	s_add_u32 s3, s20, 0x100
	s_addc_u32 s46, s21, 0
	s_add_u32 s18, s18, 0x80080
	v_mov_b32_e32 v4, 0
	s_addc_u32 s19, s19, 0
	s_mov_b32 s49, -2
	v_mov_b32_e32 v5, v4
	v_mov_b64_e32 v[6:7], v[4:5]
	v_mov_b64_e32 v[8:9], v[4:5]
	v_mov_b64_e32 v[10:11], v[4:5]
	v_mov_b64_e32 v[20:21], v[4:5]
	v_mov_b64_e32 v[22:23], v[4:5]
	v_mov_b64_e32 v[24:25], v[4:5]
	v_mov_b64_e32 v[26:27], v[4:5]
	v_mov_b64_e32 v[36:37], v[4:5]
	v_mov_b64_e32 v[38:39], v[4:5]
	v_mov_b64_e32 v[40:41], v[4:5]
	v_mov_b64_e32 v[42:43], v[4:5]
	v_mov_b64_e32 v[52:53], v[4:5]
	v_mov_b64_e32 v[54:55], v[4:5]
	v_mov_b64_e32 v[56:57], v[4:5]
	v_mov_b64_e32 v[58:59], v[4:5]
	v_mov_b64_e32 v[12:13], v[4:5]
	v_mov_b64_e32 v[14:15], v[4:5]
	v_mov_b64_e32 v[16:17], v[4:5]
	v_mov_b64_e32 v[18:19], v[4:5]
	v_mov_b64_e32 v[28:29], v[4:5]
	v_mov_b64_e32 v[30:31], v[4:5]
	v_mov_b64_e32 v[32:33], v[4:5]
	v_mov_b64_e32 v[34:35], v[4:5]
	v_mov_b64_e32 v[44:45], v[4:5]
	v_mov_b64_e32 v[46:47], v[4:5]
	v_mov_b64_e32 v[48:49], v[4:5]
	v_mov_b64_e32 v[50:51], v[4:5]
	v_mov_b64_e32 v[60:61], v[4:5]
	v_mov_b64_e32 v[62:63], v[4:5]
	v_mov_b64_e32 v[64:65], v[4:5]
	v_mov_b64_e32 v[66:67], v[4:5]
	v_mov_b64_e32 v[68:69], v[4:5]
	v_mov_b64_e32 v[70:71], v[4:5]
	v_mov_b64_e32 v[72:73], v[4:5]
	v_mov_b64_e32 v[74:75], v[4:5]
	v_mov_b64_e32 v[84:85], v[4:5]
	v_mov_b64_e32 v[86:87], v[4:5]
	v_mov_b64_e32 v[88:89], v[4:5]
	v_mov_b64_e32 v[90:91], v[4:5]
	v_mov_b64_e32 v[100:101], v[4:5]
	v_mov_b64_e32 v[102:103], v[4:5]
	v_mov_b64_e32 v[104:105], v[4:5]
	v_mov_b64_e32 v[106:107], v[4:5]
	v_mov_b64_e32 v[116:117], v[4:5]
	v_mov_b64_e32 v[118:119], v[4:5]
	v_mov_b64_e32 v[120:121], v[4:5]
	v_mov_b64_e32 v[122:123], v[4:5]
	v_mov_b64_e32 v[76:77], v[4:5]
	v_mov_b64_e32 v[78:79], v[4:5]
	v_mov_b64_e32 v[80:81], v[4:5]
	v_mov_b64_e32 v[82:83], v[4:5]
	v_mov_b64_e32 v[92:93], v[4:5]
	v_mov_b64_e32 v[94:95], v[4:5]
	v_mov_b64_e32 v[96:97], v[4:5]
	v_mov_b64_e32 v[98:99], v[4:5]
	v_mov_b64_e32 v[108:109], v[4:5]
	v_mov_b64_e32 v[110:111], v[4:5]
	v_mov_b64_e32 v[112:113], v[4:5]
	v_mov_b64_e32 v[114:115], v[4:5]
	v_mov_b64_e32 v[124:125], v[4:5]
	v_mov_b64_e32 v[126:127], v[4:5]
	v_mov_b64_e32 v[128:129], v[4:5]
	v_mov_b64_e32 v[130:131], v[4:5]

.LBB0_723:
	s_add_u32 s7, s18, 0x100
	s_addc_u32 s42, s19, 0
	s_add_u32 s16, s16, 0x80080
	v_mov_b32_e32 v4, 0
	s_addc_u32 s17, s17, 0
	s_mov_b32 s43, -2
	v_mov_b32_e32 v5, v4
	v_mov_b64_e32 v[6:7], v[4:5]
	v_mov_b64_e32 v[8:9], v[4:5]
	v_mov_b64_e32 v[10:11], v[4:5]
	v_mov_b64_e32 v[20:21], v[4:5]
	v_mov_b64_e32 v[22:23], v[4:5]
	v_mov_b64_e32 v[24:25], v[4:5]
	v_mov_b64_e32 v[26:27], v[4:5]
	v_mov_b64_e32 v[36:37], v[4:5]
	v_mov_b64_e32 v[38:39], v[4:5]
	v_mov_b64_e32 v[40:41], v[4:5]
	v_mov_b64_e32 v[42:43], v[4:5]
	v_mov_b64_e32 v[52:53], v[4:5]
	v_mov_b64_e32 v[54:55], v[4:5]
	v_mov_b64_e32 v[56:57], v[4:5]
	v_mov_b64_e32 v[58:59], v[4:5]
	v_mov_b64_e32 v[12:13], v[4:5]
	v_mov_b64_e32 v[14:15], v[4:5]
	v_mov_b64_e32 v[16:17], v[4:5]
	v_mov_b64_e32 v[18:19], v[4:5]
	v_mov_b64_e32 v[28:29], v[4:5]
	v_mov_b64_e32 v[30:31], v[4:5]
	v_mov_b64_e32 v[32:33], v[4:5]
	v_mov_b64_e32 v[34:35], v[4:5]
	v_mov_b64_e32 v[44:45], v[4:5]
	v_mov_b64_e32 v[46:47], v[4:5]
	v_mov_b64_e32 v[48:49], v[4:5]
	v_mov_b64_e32 v[50:51], v[4:5]
	v_mov_b64_e32 v[60:61], v[4:5]
	v_mov_b64_e32 v[62:63], v[4:5]
	v_mov_b64_e32 v[64:65], v[4:5]
	v_mov_b64_e32 v[66:67], v[4:5]
	v_mov_b64_e32 v[68:69], v[4:5]
	v_mov_b64_e32 v[70:71], v[4:5]
	v_mov_b64_e32 v[72:73], v[4:5]
	v_mov_b64_e32 v[74:75], v[4:5]
	v_mov_b64_e32 v[84:85], v[4:5]
	v_mov_b64_e32 v[86:87], v[4:5]
	v_mov_b64_e32 v[88:89], v[4:5]
	v_mov_b64_e32 v[90:91], v[4:5]
	v_mov_b64_e32 v[100:101], v[4:5]
	v_mov_b64_e32 v[102:103], v[4:5]
	v_mov_b64_e32 v[104:105], v[4:5]
	v_mov_b64_e32 v[106:107], v[4:5]
	v_mov_b64_e32 v[116:117], v[4:5]
	v_mov_b64_e32 v[118:119], v[4:5]
	v_mov_b64_e32 v[120:121], v[4:5]
	v_mov_b64_e32 v[122:123], v[4:5]
	v_mov_b64_e32 v[76:77], v[4:5]
	v_mov_b64_e32 v[78:79], v[4:5]
	v_mov_b64_e32 v[80:81], v[4:5]
	v_mov_b64_e32 v[82:83], v[4:5]
	v_mov_b64_e32 v[92:93], v[4:5]
	v_mov_b64_e32 v[94:95], v[4:5]
	v_mov_b64_e32 v[96:97], v[4:5]
	v_mov_b64_e32 v[98:99], v[4:5]
	v_mov_b64_e32 v[108:109], v[4:5]
	v_mov_b64_e32 v[110:111], v[4:5]
	v_mov_b64_e32 v[112:113], v[4:5]
	v_mov_b64_e32 v[114:115], v[4:5]
	v_mov_b64_e32 v[124:125], v[4:5]
	v_mov_b64_e32 v[126:127], v[4:5]
	v_mov_b64_e32 v[128:129], v[4:5]
	v_mov_b64_e32 v[130:131], v[4:5]

.LBB0_908:
	s_add_u32 s52, s22, 0x100
	s_addc_u32 s53, s23, 0
	s_add_u32 s4, s4, 0x80080
	v_mov_b32_e32 v4, 0
	s_addc_u32 s5, s5, 0
	s_mov_b32 s54, -2
	v_mov_b32_e32 v5, v4
	v_mov_b64_e32 v[6:7], v[4:5]
	v_mov_b64_e32 v[8:9], v[4:5]
	v_mov_b64_e32 v[10:11], v[4:5]
	v_mov_b64_e32 v[20:21], v[4:5]
	v_mov_b64_e32 v[22:23], v[4:5]
	v_mov_b64_e32 v[24:25], v[4:5]
	v_mov_b64_e32 v[26:27], v[4:5]
	v_mov_b64_e32 v[36:37], v[4:5]
	v_mov_b64_e32 v[38:39], v[4:5]
	v_mov_b64_e32 v[40:41], v[4:5]
	v_mov_b64_e32 v[42:43], v[4:5]
	v_mov_b64_e32 v[52:53], v[4:5]
	v_mov_b64_e32 v[54:55], v[4:5]
	v_mov_b64_e32 v[56:57], v[4:5]
	v_mov_b64_e32 v[58:59], v[4:5]
	v_mov_b64_e32 v[12:13], v[4:5]
	v_mov_b64_e32 v[14:15], v[4:5]
	v_mov_b64_e32 v[16:17], v[4:5]
	v_mov_b64_e32 v[18:19], v[4:5]
	v_mov_b64_e32 v[28:29], v[4:5]
	v_mov_b64_e32 v[30:31], v[4:5]
	v_mov_b64_e32 v[32:33], v[4:5]
	v_mov_b64_e32 v[34:35], v[4:5]
	v_mov_b64_e32 v[44:45], v[4:5]
	v_mov_b64_e32 v[46:47], v[4:5]
	v_mov_b64_e32 v[48:49], v[4:5]
	v_mov_b64_e32 v[50:51], v[4:5]
	v_mov_b64_e32 v[60:61], v[4:5]
	v_mov_b64_e32 v[62:63], v[4:5]
	v_mov_b64_e32 v[64:65], v[4:5]
	v_mov_b64_e32 v[66:67], v[4:5]
	v_mov_b64_e32 v[68:69], v[4:5]
	v_mov_b64_e32 v[70:71], v[4:5]
	v_mov_b64_e32 v[72:73], v[4:5]
	v_mov_b64_e32 v[74:75], v[4:5]
	v_mov_b64_e32 v[84:85], v[4:5]
	v_mov_b64_e32 v[86:87], v[4:5]
	v_mov_b64_e32 v[88:89], v[4:5]
	v_mov_b64_e32 v[90:91], v[4:5]
	v_mov_b64_e32 v[100:101], v[4:5]
	v_mov_b64_e32 v[102:103], v[4:5]
	v_mov_b64_e32 v[104:105], v[4:5]
	v_mov_b64_e32 v[106:107], v[4:5]
	v_mov_b64_e32 v[116:117], v[4:5]
	v_mov_b64_e32 v[118:119], v[4:5]
	v_mov_b64_e32 v[120:121], v[4:5]
	v_mov_b64_e32 v[122:123], v[4:5]
	v_mov_b64_e32 v[76:77], v[4:5]
	v_mov_b64_e32 v[78:79], v[4:5]
	v_mov_b64_e32 v[80:81], v[4:5]
	v_mov_b64_e32 v[82:83], v[4:5]
	v_mov_b64_e32 v[92:93], v[4:5]
	v_mov_b64_e32 v[94:95], v[4:5]
	v_mov_b64_e32 v[96:97], v[4:5]
	v_mov_b64_e32 v[98:99], v[4:5]
	v_mov_b64_e32 v[108:109], v[4:5]
	v_mov_b64_e32 v[110:111], v[4:5]
	v_mov_b64_e32 v[112:113], v[4:5]
	v_mov_b64_e32 v[114:115], v[4:5]
	v_mov_b64_e32 v[124:125], v[4:5]
	v_mov_b64_e32 v[126:127], v[4:5]
	v_mov_b64_e32 v[128:129], v[4:5]
	v_mov_b64_e32 v[130:131], v[4:5]

.LBB0_2114:
	s_and_b64 s[18:19], s[14:15], exec
	s_cselect_b32 s7, s3, s3
	s_cselect_b32 s45, s2, s2
	s_cselect_b32 s46, s13, s17
	s_cselect_b32 s48, s12, s16
	s_lshl_b32 s18, s41, 10
	s_add_i32 s49, s18, 0
	s_add_i32 s49, s49, 0x20800
	s_add_u32 s52, s16, 0x100
	s_addc_u32 s53, s17, 0
	s_add_u32 s16, s2, 0x80
	v_mov_b32_e32 v4, 0
	s_addc_u32 s17, s3, 0
	s_mov_b32 s54, -2
	v_mov_b32_e32 v5, v4
	v_mov_b64_e32 v[6:7], v[4:5]
	v_mov_b64_e32 v[12:13], v[4:5]
	v_mov_b64_e32 v[14:15], v[4:5]
	v_mov_b64_e32 v[20:21], v[4:5]
	v_mov_b64_e32 v[22:23], v[4:5]
	v_mov_b64_e32 v[28:29], v[4:5]
	v_mov_b64_e32 v[30:31], v[4:5]
	v_mov_b64_e32 v[36:37], v[4:5]
	v_mov_b64_e32 v[38:39], v[4:5]
	v_mov_b64_e32 v[44:45], v[4:5]
	v_mov_b64_e32 v[46:47], v[4:5]
	v_mov_b64_e32 v[52:53], v[4:5]
	v_mov_b64_e32 v[54:55], v[4:5]
	v_mov_b64_e32 v[60:61], v[4:5]
	v_mov_b64_e32 v[62:63], v[4:5]
	v_mov_b64_e32 v[8:9], v[4:5]
	v_mov_b64_e32 v[10:11], v[4:5]
	v_mov_b64_e32 v[16:17], v[4:5]
	v_mov_b64_e32 v[18:19], v[4:5]
	v_mov_b64_e32 v[24:25], v[4:5]
	v_mov_b64_e32 v[26:27], v[4:5]
	v_mov_b64_e32 v[32:33], v[4:5]
	v_mov_b64_e32 v[34:35], v[4:5]
	v_mov_b64_e32 v[40:41], v[4:5]
	v_mov_b64_e32 v[42:43], v[4:5]
	v_mov_b64_e32 v[48:49], v[4:5]
	v_mov_b64_e32 v[50:51], v[4:5]
	v_mov_b64_e32 v[56:57], v[4:5]
	v_mov_b64_e32 v[58:59], v[4:5]
	v_mov_b64_e32 v[64:65], v[4:5]
	v_mov_b64_e32 v[66:67], v[4:5]
	v_mov_b64_e32 v[68:69], v[4:5]
	v_mov_b64_e32 v[70:71], v[4:5]
	v_mov_b64_e32 v[76:77], v[4:5]
	v_mov_b64_e32 v[78:79], v[4:5]
	v_mov_b64_e32 v[84:85], v[4:5]
	v_mov_b64_e32 v[86:87], v[4:5]
	v_mov_b64_e32 v[92:93], v[4:5]
	v_mov_b64_e32 v[94:95], v[4:5]
	v_mov_b64_e32 v[100:101], v[4:5]
	v_mov_b64_e32 v[102:103], v[4:5]
	v_mov_b64_e32 v[108:109], v[4:5]
	v_mov_b64_e32 v[110:111], v[4:5]
	v_mov_b64_e32 v[116:117], v[4:5]
	v_mov_b64_e32 v[118:119], v[4:5]
	v_mov_b64_e32 v[124:125], v[4:5]
	v_mov_b64_e32 v[126:127], v[4:5]
	v_mov_b64_e32 v[72:73], v[4:5]
	v_mov_b64_e32 v[74:75], v[4:5]
	v_mov_b64_e32 v[80:81], v[4:5]
	v_mov_b64_e32 v[82:83], v[4:5]
	v_mov_b64_e32 v[88:89], v[4:5]
	v_mov_b64_e32 v[90:91], v[4:5]
	v_mov_b64_e32 v[96:97], v[4:5]
	v_mov_b64_e32 v[98:99], v[4:5]
	v_mov_b64_e32 v[104:105], v[4:5]
	v_mov_b64_e32 v[106:107], v[4:5]
	v_mov_b64_e32 v[112:113], v[4:5]
	v_mov_b64_e32 v[114:115], v[4:5]
	v_mov_b64_e32 v[120:121], v[4:5]
	v_mov_b64_e32 v[122:123], v[4:5]
	v_mov_b64_e32 v[128:129], v[4:5]
	v_mov_b64_e32 v[130:131], v[4:5]
	s_branch .LBB0_2117

.LBB0_2673:
	s_and_b64 s[34:35], s[22:23], exec
	v_mov_b32_e32 v4, 0
	s_cselect_b32 s19, s17, s27
	s_cselect_b32 s25, s16, s26
	s_cselect_b32 s46, s21, s29
	s_cselect_b32 s64, s20, s28
	s_mov_b64 s[36:37], -1
	s_mov_b64 s[34:35], 0
	v_mov_b32_e32 v5, v4
	v_mov_b64_e32 v[6:7], v[4:5]
	v_mov_b64_e32 v[8:9], v[4:5]
	v_mov_b64_e32 v[10:11], v[4:5]
	v_mov_b64_e32 v[16:17], v[4:5]
	v_mov_b64_e32 v[18:19], v[4:5]
	v_mov_b64_e32 v[24:25], v[4:5]
	v_mov_b64_e32 v[26:27], v[4:5]
	v_mov_b64_e32 v[32:33], v[4:5]
	v_mov_b64_e32 v[34:35], v[4:5]
	v_mov_b64_e32 v[40:41], v[4:5]
	v_mov_b64_e32 v[42:43], v[4:5]
	v_mov_b64_e32 v[48:49], v[4:5]
	v_mov_b64_e32 v[50:51], v[4:5]
	v_mov_b64_e32 v[56:57], v[4:5]
	v_mov_b64_e32 v[58:59], v[4:5]
	v_mov_b64_e32 v[12:13], v[4:5]
	v_mov_b64_e32 v[14:15], v[4:5]
	v_mov_b64_e32 v[20:21], v[4:5]
	v_mov_b64_e32 v[22:23], v[4:5]
	v_mov_b64_e32 v[28:29], v[4:5]
	v_mov_b64_e32 v[30:31], v[4:5]
	v_mov_b64_e32 v[36:37], v[4:5]
	v_mov_b64_e32 v[38:39], v[4:5]
	v_mov_b64_e32 v[44:45], v[4:5]
	v_mov_b64_e32 v[46:47], v[4:5]
	v_mov_b64_e32 v[52:53], v[4:5]
	v_mov_b64_e32 v[54:55], v[4:5]
	v_mov_b64_e32 v[60:61], v[4:5]
	v_mov_b64_e32 v[62:63], v[4:5]
	v_mov_b64_e32 v[64:65], v[4:5]
	v_mov_b64_e32 v[66:67], v[4:5]
	v_mov_b64_e32 v[68:69], v[4:5]
	v_mov_b64_e32 v[70:71], v[4:5]
	v_mov_b64_e32 v[72:73], v[4:5]
	v_mov_b64_e32 v[74:75], v[4:5]
	v_mov_b64_e32 v[80:81], v[4:5]
	v_mov_b64_e32 v[82:83], v[4:5]
	v_mov_b64_e32 v[88:89], v[4:5]
	v_mov_b64_e32 v[90:91], v[4:5]
	v_mov_b64_e32 v[96:97], v[4:5]
	v_mov_b64_e32 v[98:99], v[4:5]
	v_mov_b64_e32 v[104:105], v[4:5]
	v_mov_b64_e32 v[106:107], v[4:5]
	v_mov_b64_e32 v[112:113], v[4:5]
	v_mov_b64_e32 v[114:115], v[4:5]
	v_mov_b64_e32 v[120:121], v[4:5]
	v_mov_b64_e32 v[122:123], v[4:5]
	v_mov_b64_e32 v[76:77], v[4:5]
	v_mov_b64_e32 v[78:79], v[4:5]
	v_mov_b64_e32 v[84:85], v[4:5]
	v_mov_b64_e32 v[86:87], v[4:5]
	v_mov_b64_e32 v[92:93], v[4:5]
	v_mov_b64_e32 v[94:95], v[4:5]
	v_mov_b64_e32 v[100:101], v[4:5]
	v_mov_b64_e32 v[102:103], v[4:5]
	v_mov_b64_e32 v[108:109], v[4:5]
	v_mov_b64_e32 v[110:111], v[4:5]
	v_mov_b64_e32 v[116:117], v[4:5]
	v_mov_b64_e32 v[118:119], v[4:5]
	v_mov_b64_e32 v[124:125], v[4:5]
	v_mov_b64_e32 v[126:127], v[4:5]
	v_mov_b64_e32 v[128:129], v[4:5]
	v_mov_b64_e32 v[130:131], v[4:5]
